# nt hint also on the gating-unit output (consumed three phases later) and the compression-MLP weight stores in the prologue
# speedup vs baseline: 1.0111x; 1.0052x over previous
; __device__ __forceinline__ unsigned cvt_pk_bf16(float lo, float hi) { f32x2_t v = {lo, hi}; bf16x2_t b = __builtin_convertvector(v, bf16x2_t); return __builtin_bit_cast(unsigned, b); }
;     const int c = lane & 7, nn = lane >> 3;
;     const float* src0 = W + (size_t)(kb * 64 + 8 * c) * ldw;
; #pragma unroll 2
;     for (int sb = sb0; sb < sb1; ++sb) {
;         const int n = nb * 256 + sb * 32 + 4 * nn;
;         if (n < N) {
;             int r = n;
;             if (rowmode == 1) r = n < 2608 ? n : n + 208;
;             else if (rowmode == 2) r = ((n >> 7) << 8) + (n & 127);
;             else if (rowmode == 3) r = ((n >> 7) << 8) + 128 + (n & 127);
;             const float* src = src0 + n;
;             f32x4 v[8];
; #pragma unroll
;             for (int i = 0; i < 8; ++i) v[i] = *(const f32x4*)(src + (size_t)i * ldw);
;             bf16* d0 = WT + (size_t)r * K + kb * 64 + 8 * c;
; #pragma unroll
;             for (int j = 0; j < 4; ++j) { u32x4 o; o.x = cvt_pk_bf16(v[0][j], v[1][j]); o.y = cvt_pk_bf16(v[2][j], v[3][j]); o.z = cvt_pk_bf16(v[4][j], v[5][j]); o.w = cvt_pk_bf16(v[6][j], v[7][j]);
;                 *(u32x4*)(d0 + (size_t)j * K) = o; }
;         }
;     }
; }
; __global__ void __launch_bounds__(NWAVES * 64, 2) trunk_fwd(Args args) {
;     ...
;                 if (r < C_CW2) { const int lk = r / 4, q = r % 4; conv_tile(args.in[(lk & 1) ? I_VW2 : I_KW2] + (size_t)(lk >> 1) * 256 * 64, 64, 256, 64, CW2_T + (size_t)lk * 64 * 256, 0, q, 0, lane, wave, wave + 1); continue; } r -= C_CW2;
.LBB0_38:
	s_andn2_b64 vcc, exec, s[20:21]
	s_cbranch_vccnz .LBB0_41
	s_andn2_b64 vcc, exec, s[14:15]
	s_cbranch_vccnz .LBB0_41
	s_add_i32 s2, s67, 0xfffff2c0
	s_lshr_b32 s18, s2, 2
	s_lshl_b64 s[20:21], s[18:19], 15
	s_add_u32 s18, s22, s20
	s_addc_u32 s21, s23, s21
	s_and_b32 s70, s35, 0xc0
	s_lshl_b32 s20, s70, 1
	s_add_u32 s20, s18, s20
	s_addc_u32 s21, s21, 0
	s_bitcmp0_b32 s67, 2
	s_cselect_b32 s18, 48, 64
	s_add_u32 s68, s0, s18
	s_addc_u32 s69, s1, 0
	s_load_dwordx2 s[68:69], s[68:69], 0x0
	v_lshlrev_b32_e32 v4, 1, v2
	s_lshr_b32 s18, s2, 3
	v_lshl_add_u64 v[50:51], s[20:21], 0, v[4:5]
	s_lshl_b64 s[20:21], s[18:19], 16
	s_waitcnt lgkmcnt(0)
	s_add_u32 s20, s68, s20
	v_or_b32_e32 v4, s70, v2
	s_addc_u32 s21, s69, s21
	v_lshlrev_b32_e32 v4, 8, v4
	v_lshl_add_u64 v[18:19], s[20:21], 0, v[4:5]
	v_lshl_add_u64 v[46:47], v[10:11], 2, v[18:19]
	global_load_dwordx4 v[18:21], v[46:47], off nt
	global_load_dwordx4 v[22:25], v[46:47], off offset:256 nt
	global_load_dwordx4 v[26:29], v[46:47], off offset:512 nt
	global_load_dwordx4 v[30:33], v[46:47], off offset:768 nt
	global_load_dwordx4 v[34:37], v[46:47], off offset:1024 nt
	global_load_dwordx4 v[38:41], v[46:47], off offset:1280 nt
	global_load_dwordx4 v[42:45], v[46:47], off offset:1536 nt
	s_nop 0
	global_load_dwordx4 v[46:49], v[46:47], off offset:1792 nt
	v_lshl_add_u64 v[62:63], v[50:51], 0, v[12:13]
	s_waitcnt vmcnt(6)
	v_cvt_pk_bf16_f32 v50, v18, v22
	v_cvt_pk_bf16_f32 v54, v19, v23
	s_waitcnt vmcnt(4)
	v_cvt_pk_bf16_f32 v51, v26, v30
	v_cvt_pk_bf16_f32 v55, v27, v31
	s_waitcnt vmcnt(2)
	v_cvt_pk_bf16_f32 v52, v34, v38
	v_cvt_pk_bf16_f32 v56, v35, v39
	s_waitcnt vmcnt(0)
	v_cvt_pk_bf16_f32 v53, v42, v46
	v_cvt_pk_bf16_f32 v57, v43, v47
	v_cvt_pk_bf16_f32 v58, v20, v24
	v_cvt_pk_bf16_f32 v59, v28, v32
	v_cvt_pk_bf16_f32 v60, v36, v40
	v_cvt_pk_bf16_f32 v61, v44, v48
	v_cvt_pk_bf16_f32 v18, v21, v25
	v_cvt_pk_bf16_f32 v19, v29, v33
	v_cvt_pk_bf16_f32 v20, v37, v41
	v_cvt_pk_bf16_f32 v21, v45, v49
	global_store_dwordx4 v[62:63], v[50:53], off nt
	global_store_dwordx4 v[62:63], v[54:57], off offset:512 nt
	global_store_dwordx4 v[62:63], v[58:61], off offset:1024 nt
	global_store_dwordx4 v[62:63], v[18:21], off offset:1536 nt

; __device__ __forceinline__ unsigned cvt_pk_bf16(float lo, float hi) { f32x2_t v = {lo, hi}; bf16x2_t b = __builtin_convertvector(v, bf16x2_t); return __builtin_bit_cast(unsigned, b); }
;     const int c = lane & 7, nn = lane >> 3;
;     const float* src0 = W + (size_t)(kb * 64 + 8 * c) * ldw;
; #pragma unroll 2
;     for (int sb = sb0; sb < sb1; ++sb) {
;         const int n = nb * 256 + sb * 32 + 4 * nn;
;         if (n < N) {
;             int r = n;
;             if (rowmode == 1) r = n < 2608 ? n : n + 208;
;             else if (rowmode == 2) r = ((n >> 7) << 8) + (n & 127);
;             else if (rowmode == 3) r = ((n >> 7) << 8) + 128 + (n & 127);
;             const float* src = src0 + n;
;             f32x4 v[8];
; #pragma unroll
;             for (int i = 0; i < 8; ++i) v[i] = *(const f32x4*)(src + (size_t)i * ldw);
;             bf16* d0 = WT + (size_t)r * K + kb * 64 + 8 * c;
; #pragma unroll
;             for (int j = 0; j < 4; ++j) { u32x4 o; o.x = cvt_pk_bf16(v[0][j], v[1][j]); o.y = cvt_pk_bf16(v[2][j], v[3][j]); o.z = cvt_pk_bf16(v[4][j], v[5][j]); o.w = cvt_pk_bf16(v[6][j], v[7][j]);
;                 *(u32x4*)(d0 + (size_t)j * K) = o; }
;         }
;     }
; }
; __global__ void __launch_bounds__(NWAVES * 64, 2) trunk_fwd(Args args) {
;     ...
;                 if (r < C_CW1) { const int lk = r / 32, q = r % 32; conv_tile(args.in[(lk & 1) ? I_VW1 : I_KW1] + (size_t)(lk >> 1) * 2048 * 256, 256, 2048, 256, CW1_T + (size_t)lk * 256 * 2048, 0, q, 0, lane, wave, wave + 1); continue; } r -= C_CW1;
.LBB0_42:
	s_andn2_b64 vcc, exec, s[20:21]
	s_cbranch_vccnz .LBB0_45
	s_andn2_b64 vcc, exec, s[16:17]
	s_cbranch_vccnz .LBB0_45
	s_add_i32 s2, s67, 0xfffff340
	s_lshr_b32 s18, s2, 5
	s_lshl_b64 s[20:21], s[18:19], 20
	s_add_u32 s18, s24, s20
	s_addc_u32 s21, s25, s21
	s_and_b32 s70, s35, 0x7c0
	s_lshl_b32 s20, s70, 1
	s_add_u32 s20, s18, s20
	s_addc_u32 s21, s21, 0
	s_bitcmp0_b32 s67, 5
	s_cselect_b32 s18, 40, 56
	s_add_u32 s68, s0, s18
	s_addc_u32 s69, s1, 0
	s_load_dwordx2 s[68:69], s[68:69], 0x0
	v_lshlrev_b32_e32 v4, 1, v2
	s_lshr_b32 s18, s2, 6
	v_lshl_add_u64 v[50:51], s[20:21], 0, v[4:5]
	s_lshl_b64 s[20:21], s[18:19], 21
	s_waitcnt lgkmcnt(0)
	s_add_u32 s20, s68, s20
	v_or_b32_e32 v4, s70, v2
	s_addc_u32 s21, s69, s21
	v_lshlrev_b32_e32 v4, 10, v4
	v_lshl_add_u64 v[18:19], s[20:21], 0, v[4:5]
	v_lshl_add_u64 v[34:35], v[10:11], 2, v[18:19]
	v_add_co_u32_e32 v46, vcc, s55, v34
	global_load_dwordx4 v[18:21], v[34:35], off nt
	global_load_dwordx4 v[22:25], v[34:35], off offset:1024 nt
	global_load_dwordx4 v[26:29], v[34:35], off offset:2048 nt
	global_load_dwordx4 v[30:33], v[34:35], off offset:3072 nt
	v_addc_co_u32_e32 v47, vcc, 0, v35, vcc
	global_load_dwordx4 v[34:37], v[46:47], off nt
	global_load_dwordx4 v[38:41], v[46:47], off offset:1024 nt
	global_load_dwordx4 v[42:45], v[46:47], off offset:2048 nt
	s_nop 0
	global_load_dwordx4 v[46:49], v[46:47], off offset:3072 nt
	v_lshl_add_u64 v[54:55], v[50:51], 0, v[14:15]
	v_add_co_u32_e32 v56, vcc, s37, v54
	s_waitcnt vmcnt(6)
	v_cvt_pk_bf16_f32 v50, v18, v22
	v_addc_co_u32_e32 v57, vcc, 0, v55, vcc
	v_add_co_u32_e32 v58, vcc, 0x3000, v54
	s_waitcnt vmcnt(4)
	v_cvt_pk_bf16_f32 v51, v26, v30
	s_waitcnt vmcnt(2)
	v_cvt_pk_bf16_f32 v52, v34, v38
	s_waitcnt vmcnt(0)
	v_cvt_pk_bf16_f32 v53, v42, v46
	v_addc_co_u32_e32 v59, vcc, 0, v55, vcc
	v_cvt_pk_bf16_f32 v18, v19, v23
	v_cvt_pk_bf16_f32 v19, v27, v31
	v_cvt_pk_bf16_f32 v22, v20, v24
	v_cvt_pk_bf16_f32 v23, v28, v32
	v_cvt_pk_bf16_f32 v26, v21, v25
	v_cvt_pk_bf16_f32 v27, v29, v33
	v_cvt_pk_bf16_f32 v20, v35, v39
	v_cvt_pk_bf16_f32 v21, v43, v47
	v_cvt_pk_bf16_f32 v24, v36, v40
	v_cvt_pk_bf16_f32 v25, v44, v48
	v_cvt_pk_bf16_f32 v28, v37, v41
	v_cvt_pk_bf16_f32 v29, v45, v49
	global_store_dwordx4 v[54:55], v[50:53], off nt
	global_store_dwordx4 v[56:57], v[18:21], off offset:-4096 nt
	global_store_dwordx4 v[56:57], v[22:25], off nt
	global_store_dwordx4 v[58:59], v[26:29], off nt

; #define LAS __attribute__((address_space(3)))
; __device__ __forceinline__ unsigned f2bf(float f) { unsigned u = __builtin_bit_cast(unsigned, f); return (u + 0x7fffu + ((u >> 16) & 1u)) >> 16; }
; __device__ __forceinline__ int crow(int r, int hi) { return (r & 3) + 8 * (r >> 2) + 4 * hi; }
; __device__ __forceinline__ void unit(LAS unsigned char* lds, const bf16* Z, const bf16* sgw, const float* lng, const float* lnb, const float* sgb, bf16* OBp, int b, int nchunk, int g0, int ng, const int tid_in) {
;     ...
;         for (int x = 0; x < 2; ++x)
; #pragma unroll
;             for (int r = 0; r < 16; ++r) { const int tt = 32 * tb + crow(r, hi); LAS bf16* up = UL + tt * ST + 32 * (dbase + x) + r32;
;                 *up = (bf16)f2bf(bf2f(*up) * (acc[x][r] + BL[tt])); }
.LBB0_295:
	ds_read_u16 v34, v101
	s_add_i32 s14, s21, 1
	s_cmp_eq_u32 s21, s22
	s_mov_b32 s21, s14
	s_waitcnt lgkmcnt(0)
	v_lshlrev_b32_e32 v38, 16, v34
	ds_read_b128 v[34:37], v94
	s_waitcnt lgkmcnt(0)
	v_add_f32_e32 v18, v18, v34
	v_mul_f32_e32 v18, v18, v38
	v_bfe_u32 v38, v18, 16, 1
	v_add3_u32 v18, v18, v38, s36
	ds_write_b16_d16_hi v101, v18
	ds_read_u16 v18, v101 offset:272
	v_add_f32_e32 v19, v19, v35
	v_add_f32_e32 v2, v2, v34
	v_add_f32_e32 v3, v3, v35
	s_waitcnt lgkmcnt(0)
	v_lshlrev_b32_e32 v18, 16, v18
	v_mul_f32_e32 v18, v19, v18
	v_bfe_u32 v19, v18, 16, 1
	v_add3_u32 v18, v18, v19, s36
	ds_write_b16_d16_hi v101, v18 offset:272
	ds_read_u16 v18, v101 offset:544
	v_add_f32_e32 v19, v20, v36
	s_waitcnt lgkmcnt(0)
	v_lshlrev_b32_e32 v18, 16, v18
	v_mul_f32_e32 v18, v19, v18
	v_bfe_u32 v19, v18, 16, 1
	v_add3_u32 v18, v18, v19, s36
	ds_write_b16_d16_hi v101, v18 offset:544
	ds_read_u16 v18, v101 offset:816
	v_add_f32_e32 v19, v21, v37
	s_waitcnt lgkmcnt(0)
	v_lshlrev_b32_e32 v18, 16, v18
	v_mul_f32_e32 v18, v19, v18
	v_bfe_u32 v19, v18, 16, 1
	v_add3_u32 v18, v18, v19, s36
	ds_write_b16_d16_hi v101, v18 offset:816
	ds_read_u16 v18, v101 offset:2176
	s_waitcnt lgkmcnt(0)
	v_lshlrev_b32_e32 v38, 16, v18
	ds_read_b128 v[18:21], v95
	s_waitcnt lgkmcnt(0)
	v_add_f32_e32 v22, v22, v18
	v_mul_f32_e32 v22, v22, v38
	v_bfe_u32 v38, v22, 16, 1
	v_add3_u32 v22, v22, v38, s36
	ds_write_b16_d16_hi v101, v22 offset:2176
	ds_read_u16 v22, v101 offset:2448
	ds_read_b128 v[38:41], v96
	v_add_f32_e32 v23, v23, v19
	s_waitcnt lgkmcnt(1)
	v_lshlrev_b32_e32 v22, 16, v22
	v_mul_f32_e32 v22, v23, v22
	v_bfe_u32 v23, v22, 16, 1
	v_add3_u32 v22, v22, v23, s36
	ds_write_b16_d16_hi v101, v22 offset:2448
	ds_read_u16 v22, v101 offset:2720
	v_add_f32_e32 v23, v24, v20
	s_waitcnt lgkmcnt(0)
	v_lshlrev_b32_e32 v22, 16, v22
	v_mul_f32_e32 v22, v23, v22
	v_bfe_u32 v23, v22, 16, 1
	v_add3_u32 v22, v22, v23, s36
	ds_write_b16_d16_hi v101, v22 offset:2720
	ds_read_u16 v22, v101 offset:2992
	v_add_f32_e32 v23, v25, v21
	s_waitcnt lgkmcnt(0)
	v_lshlrev_b32_e32 v22, 16, v22
	v_mul_f32_e32 v22, v23, v22
	v_bfe_u32 v23, v22, 16, 1
	v_add3_u32 v22, v22, v23, s36
	ds_write_b16_d16_hi v101, v22 offset:2992
	ds_read_u16 v22, v101 offset:4352
	v_add_f32_e32 v23, v26, v38
	s_waitcnt lgkmcnt(0)
	v_lshlrev_b32_e32 v22, 16, v22
	v_mul_f32_e32 v22, v23, v22
	v_bfe_u32 v23, v22, 16, 1
	v_add3_u32 v22, v22, v23, s36
	ds_write_b16_d16_hi v101, v22 offset:4352
	ds_read_u16 v22, v101 offset:4624
	v_add_f32_e32 v23, v27, v39
	s_waitcnt lgkmcnt(0)
	v_lshlrev_b32_e32 v22, 16, v22
	v_mul_f32_e32 v22, v23, v22
	v_bfe_u32 v23, v22, 16, 1
	v_add3_u32 v22, v22, v23, s36
	ds_write_b16_d16_hi v101, v22 offset:4624
	ds_read_u16 v22, v101 offset:4896
	v_add_f32_e32 v23, v28, v40
	s_waitcnt lgkmcnt(0)
	v_lshlrev_b32_e32 v22, 16, v22
	v_mul_f32_e32 v22, v23, v22
	v_bfe_u32 v23, v22, 16, 1
	v_add3_u32 v22, v22, v23, s36
	ds_write_b16_d16_hi v101, v22 offset:4896
	ds_read_u16 v22, v101 offset:5168
	v_add_f32_e32 v23, v29, v41
	s_waitcnt lgkmcnt(0)
	v_lshlrev_b32_e32 v22, 16, v22
	v_mul_f32_e32 v22, v23, v22
	v_bfe_u32 v23, v22, 16, 1
	v_add3_u32 v22, v22, v23, s36
	ds_write_b16_d16_hi v101, v22 offset:5168
	ds_read_u16 v22, v101 offset:6528
	s_waitcnt lgkmcnt(0)
	v_lshlrev_b32_e32 v26, 16, v22
	ds_read_b128 v[22:25], v97
	s_waitcnt lgkmcnt(0)
	v_add_f32_e32 v27, v30, v22
	v_mul_f32_e32 v26, v27, v26
	v_bfe_u32 v27, v26, 16, 1
	v_add3_u32 v26, v26, v27, s36
	ds_write_b16_d16_hi v101, v26 offset:6528
	ds_read_u16 v26, v101 offset:6800
	v_add_f32_e32 v27, v31, v23
	s_waitcnt lgkmcnt(0)
	v_lshlrev_b32_e32 v26, 16, v26
	v_mul_f32_e32 v26, v27, v26
	v_bfe_u32 v27, v26, 16, 1
	v_add3_u32 v26, v26, v27, s36
	ds_write_b16_d16_hi v101, v26 offset:6800
	ds_read_u16 v26, v101 offset:7072
	v_add_f32_e32 v27, v32, v24
	s_waitcnt lgkmcnt(0)
	v_lshlrev_b32_e32 v26, 16, v26
	v_mul_f32_e32 v26, v27, v26
	v_bfe_u32 v27, v26, 16, 1
	v_add3_u32 v26, v26, v27, s36
	ds_write_b16_d16_hi v101, v26 offset:7072
	ds_read_u16 v26, v101 offset:7344
	v_add_f32_e32 v27, v33, v25
	s_waitcnt lgkmcnt(0)
	v_lshlrev_b32_e32 v26, 16, v26
	v_mul_f32_e32 v26, v27, v26
	v_bfe_u32 v27, v26, 16, 1
	v_add3_u32 v26, v26, v27, s36
	ds_write_b16_d16_hi v101, v26 offset:7344
	ds_read_u16 v26, v102
	s_waitcnt lgkmcnt(0)
; #define LAS __attribute__((address_space(3)))
; __device__ __forceinline__ unsigned f2bf(float f) { unsigned u = __builtin_bit_cast(unsigned, f); return (u + 0x7fffu + ((u >> 16) & 1u)) >> 16; }
; __device__ __forceinline__ int crow(int r, int hi) { return (r & 3) + 8 * (r >> 2) + 4 * hi; }
; __device__ __forceinline__ void unit(LAS unsigned char* lds, const bf16* Z, const bf16* sgw, const float* lng, const float* lnb, const float* sgb, bf16* OBp, int b, int nchunk, int g0, int ng, const int tid_in) {
;     ...
;         for (int x = 0; x < 2; ++x)
; #pragma unroll
;             for (int r = 0; r < 16; ++r) { const int tt = 32 * tb + crow(r, hi); LAS bf16* up = UL + tt * ST + 32 * (dbase + x) + r32;
;                 *up = (bf16)f2bf(bf2f(*up) * (acc[x][r] + BL[tt])); }
;         __syncthreads();
; #pragma unroll
;         for (int q = 0; q < 4; ++q) { const int idx = tid + 512 * q, row = idx >> 4, ch = idx & 15;
;             *(v4u*)(OBp + (size_t)(tb0 + row) * 1024 + g * 128 + ch * 8) = *(const LAS v4u*)(UL + row * ST + ch * 8); }
;         __syncthreads();
	v_lshlrev_b32_e32 v26, 16, v26
	v_mul_f32_e32 v2, v2, v26
	v_bfe_u32 v26, v2, 16, 1
	v_add3_u32 v2, v2, v26, s36
	ds_write_b16_d16_hi v102, v2
	ds_read_u16 v2, v102 offset:272
	s_waitcnt lgkmcnt(0)
	v_lshlrev_b32_e32 v2, 16, v2
	v_mul_f32_e32 v2, v3, v2
	v_bfe_u32 v3, v2, 16, 1
	v_add3_u32 v2, v2, v3, s36
	ds_write_b16_d16_hi v102, v2 offset:272
	ds_read_u16 v2, v102 offset:544
	v_add_f32_e32 v3, v4, v36
	s_waitcnt lgkmcnt(0)
	v_lshlrev_b32_e32 v2, 16, v2
	v_mul_f32_e32 v2, v3, v2
	v_bfe_u32 v3, v2, 16, 1
	v_add3_u32 v2, v2, v3, s36
	ds_write_b16_d16_hi v102, v2 offset:544
	ds_read_u16 v2, v102 offset:816
	v_add_f32_e32 v3, v5, v37
	s_waitcnt lgkmcnt(0)
	v_lshlrev_b32_e32 v2, 16, v2
	v_mul_f32_e32 v2, v3, v2
	v_bfe_u32 v3, v2, 16, 1
	v_add3_u32 v2, v2, v3, s36
	ds_write_b16_d16_hi v102, v2 offset:816
	ds_read_u16 v2, v102 offset:2176
	v_add_f32_e32 v3, v6, v18
	s_waitcnt lgkmcnt(0)
	v_lshlrev_b32_e32 v2, 16, v2
	v_mul_f32_e32 v2, v3, v2
	v_bfe_u32 v3, v2, 16, 1
	v_add3_u32 v2, v2, v3, s36
	ds_write_b16_d16_hi v102, v2 offset:2176
	ds_read_u16 v2, v102 offset:2448
	v_add_f32_e32 v3, v7, v19
	v_lshl_add_u64 v[6:7], s[28:29], 1, v[44:45]
	s_waitcnt lgkmcnt(0)
	v_lshlrev_b32_e32 v2, 16, v2
	v_mul_f32_e32 v2, v3, v2
	v_bfe_u32 v3, v2, 16, 1
	v_add3_u32 v2, v2, v3, s36
	ds_write_b16_d16_hi v102, v2 offset:2448
	ds_read_u16 v2, v102 offset:2720
	v_add_f32_e32 v3, v8, v20
	s_waitcnt lgkmcnt(0)
	v_lshlrev_b32_e32 v2, 16, v2
	v_mul_f32_e32 v2, v3, v2
	v_bfe_u32 v3, v2, 16, 1
	v_add3_u32 v2, v2, v3, s36
	ds_write_b16_d16_hi v102, v2 offset:2720
	ds_read_u16 v2, v102 offset:2992
	v_add_f32_e32 v3, v9, v21
	v_lshl_add_u64 v[8:9], v[6:7], 0, v[62:63]
	s_waitcnt lgkmcnt(0)
	v_lshlrev_b32_e32 v2, 16, v2
	v_mul_f32_e32 v2, v3, v2
	v_bfe_u32 v3, v2, 16, 1
	v_add3_u32 v2, v2, v3, s36
	ds_write_b16_d16_hi v102, v2 offset:2992
	ds_read_u16 v2, v102 offset:4352
	v_add_f32_e32 v3, v10, v38
	s_waitcnt lgkmcnt(0)
	v_lshlrev_b32_e32 v2, 16, v2
	v_mul_f32_e32 v2, v3, v2
	v_bfe_u32 v3, v2, 16, 1
	v_add3_u32 v2, v2, v3, s36
	ds_write_b16_d16_hi v102, v2 offset:4352
	ds_read_u16 v2, v102 offset:4624
	v_add_f32_e32 v3, v11, v39
	s_waitcnt lgkmcnt(0)
	v_lshlrev_b32_e32 v2, 16, v2
	v_mul_f32_e32 v2, v3, v2
	v_bfe_u32 v3, v2, 16, 1
	v_add3_u32 v2, v2, v3, s36
	ds_write_b16_d16_hi v102, v2 offset:4624
	ds_read_u16 v2, v102 offset:4896
	v_add_f32_e32 v3, v12, v40
	s_waitcnt lgkmcnt(0)
	v_lshlrev_b32_e32 v2, 16, v2
	v_mul_f32_e32 v2, v3, v2
	v_bfe_u32 v3, v2, 16, 1
	v_add3_u32 v2, v2, v3, s36
	ds_write_b16_d16_hi v102, v2 offset:4896
	ds_read_u16 v2, v102 offset:5168
	v_add_f32_e32 v3, v13, v41
	s_waitcnt lgkmcnt(0)
	v_lshlrev_b32_e32 v2, 16, v2
	v_mul_f32_e32 v2, v3, v2
	v_bfe_u32 v3, v2, 16, 1
	v_add3_u32 v2, v2, v3, s36
	ds_write_b16_d16_hi v102, v2 offset:5168
	ds_read_u16 v2, v102 offset:6528
	v_add_f32_e32 v3, v14, v22
	s_waitcnt lgkmcnt(0)
	v_lshlrev_b32_e32 v2, 16, v2
	v_mul_f32_e32 v2, v3, v2
	v_bfe_u32 v3, v2, 16, 1
	v_add3_u32 v2, v2, v3, s36
	ds_write_b16_d16_hi v102, v2 offset:6528
	ds_read_u16 v2, v102 offset:6800
	v_add_f32_e32 v3, v15, v23
	s_waitcnt lgkmcnt(0)
	v_lshlrev_b32_e32 v2, 16, v2
	v_mul_f32_e32 v2, v3, v2
	v_bfe_u32 v3, v2, 16, 1
	v_add3_u32 v2, v2, v3, s36
	ds_write_b16_d16_hi v102, v2 offset:6800
	ds_read_u16 v2, v102 offset:7072
	v_add_f32_e32 v3, v16, v24
	s_waitcnt lgkmcnt(0)
	v_lshlrev_b32_e32 v2, 16, v2
	v_mul_f32_e32 v2, v3, v2
	v_bfe_u32 v3, v2, 16, 1
	v_add3_u32 v2, v2, v3, s36
	ds_write_b16_d16_hi v102, v2 offset:7072
	ds_read_u16 v2, v102 offset:7344
	v_add_f32_e32 v3, v17, v25
	s_waitcnt lgkmcnt(0)
	v_lshlrev_b32_e32 v2, 16, v2
	v_mul_f32_e32 v2, v3, v2
	v_bfe_u32 v3, v2, 16, 1
	v_add3_u32 v2, v2, v3, s36
	ds_write_b16_d16_hi v102, v2 offset:7344
	s_waitcnt lgkmcnt(0)
	s_barrier
	ds_read_b128 v[2:5], v103
	s_waitcnt lgkmcnt(0)
	global_store_dwordx4 v[8:9], v[2:5], off nt
	ds_read_b128 v[2:5], v81
	v_lshl_add_u64 v[8:9], v[6:7], 0, v[64:65]
	s_waitcnt lgkmcnt(0)
	global_store_dwordx4 v[8:9], v[2:5], off nt
	ds_read_b128 v[2:5], v86
	v_lshl_add_u64 v[8:9], v[6:7], 0, v[66:67]
	v_lshl_add_u64 v[6:7], v[6:7], 0, v[68:69]
	s_waitcnt lgkmcnt(0)
	global_store_dwordx4 v[8:9], v[2:5], off nt
	ds_read_b128 v[2:5], v91
	s_waitcnt lgkmcnt(0)
	global_store_dwordx4 v[6:7], v[2:5], off nt
	s_barrier
	s_cbranch_scc1 .LBB0_288
